# barriers in front of the input-projection and down-projection GEMMs arrive-only; their completion is awaited in the GEMM prologue after the first two weight-tile stages are issued
# speedup vs baseline: 1.0058x; 1.0058x over previous
.LBB0_173:
	s_or_b64 exec, exec, s[8:9]
	v_cvt_f32_u32_e32 v4, v2
	s_waitcnt vmcnt(1)
	v_readfirstlane_b32 s4, v3
	v_sub_u32_e32 v3, 0, v2
	v_rcp_iflag_f32_e32 v4, v4
	v_add_u32_e32 v5, s4, v1
	v_mul_f32_e32 v4, 0x4f7ffffe, v4
	v_cvt_u32_f32_e32 v4, v4
	v_mul_lo_u32 v1, v3, v4
	v_mul_hi_u32 v1, v4, v1
	v_add_u32_e32 v1, v4, v1
	v_mul_hi_u32 v1, v5, v1
	v_mul_lo_u32 v3, v1, v2
	v_sub_u32_e32 v3, v5, v3
	v_add_u32_e32 v4, 1, v1
	v_cmp_ge_u32_e32 vcc, v3, v2
	s_nop 1
	v_cndmask_b32_e32 v1, v1, v4, vcc
	v_sub_u32_e32 v4, v3, v2
	v_cndmask_b32_e32 v3, v3, v4, vcc
	v_add_u32_e32 v4, 1, v1
	v_cmp_ge_u32_e32 vcc, v3, v2
	v_add_u32_e32 v3, 1, v5
	s_nop 0
	v_cndmask_b32_e32 v1, v1, v4, vcc
	v_mul_lo_u32 v4, v2, v1
	v_add_u32_e32 v2, v4, v2
	v_readlane_b32 s100, v235, 7
	v_readlane_b32 s101, v235, 8
	v_add_u32_e32 v236, 1, v1
	s_waitcnt lgkmcnt(0)
	v_mul_lo_u32 v236, v236, v0
	v_mov_b32_e32 v237, 0x3400
	v_mov_b32_e32 v239, 0
	v_cmp_ne_u32_e32 vcc, v3, v2
	s_cbranch_vccnz .Lxb_poll_1
	buffer_wbl2 sc1
	s_waitcnt vmcnt(0)
	v_mov_b32_e32 v238, 1
	global_atomic_add v237, v238, s[100:101]
.Lxb_poll_1:
	v_readfirstlane_b32 s98, v236
	s_branch .Lxb_done_1

.LBB0_211:
	s_andn2_b64 vcc, exec, s[2:3]
	v_readlane_b32 s16, v235, 16
	v_readlane_b32 s17, v235, 17
	s_cbranch_vccnz .LBB0_265
	v_ashrrev_i32_e32 v1, 31, v8
	v_lshrrev_b32_e32 v1, 26, v1
	v_add_u32_e32 v1, v8, v1
	v_ashrrev_i32_e32 v9, 6, v1
	v_bfe_i32 v1, v8, 27, 1
	v_lshlrev_b32_e32 v0, 4, v8
	v_lshrrev_b32_e32 v1, 22, v1
	v_add_u32_e32 v1, v0, v1
	v_and_b32_e32 v1, 0xfffffc00, v1
	v_sub_u32_e32 v1, v0, v1
	v_lshrrev_b32_e32 v2, 4, v1
	v_bitop3_b32 v2, v2, v1, 32 bitop3:0x6c
	v_ashrrev_i32_e32 v1, 31, v1
	v_lshrrev_b32_e32 v1, 26, v1
	v_add_u32_e32 v1, v2, v1
	v_ashrrev_i32_e32 v10, 6, v1
	v_lshlrev_b32_e32 v3, 3, v9
	v_mul_i32_i24_e32 v4, 64, v10
	v_and_b32_e32 v3, -16, v3
	v_sub_u32_e32 v2, v2, v4
	v_mov_b32_e32 v4, 1
	v_add_u32_e32 v1, v10, v3
	v_lshlrev_b32_e32 v3, 5, v9
	v_ashrrev_i16_sdwa v2, v4, sext(v2) dst_sel:DWORD dst_unused:UNUSED_PAD src0_sel:DWORD src1_sel:BYTE_0
	v_and_b32_e32 v3, 32, v3
	v_bfe_i32 v11, v2, 0, 16
	v_and_b32_e32 v6, 3, v10
	s_mov_b32 s9, 0x1fffe0
	v_add_lshl_u32 v3, v3, v11, 1
	v_add_u32_e32 v0, 0x2000, v0
	v_lshlrev_b32_e32 v2, 1, v1
	v_lshrrev_b32_e32 v5, 2, v1
	v_and_or_b32 v6, v1, s9, v6
	v_lshl_add_u32 v138, v1, 11, v3
	v_ashrrev_i32_e32 v1, 31, v0
	v_lshrrev_b32_e32 v1, 22, v1
	v_add_u32_e32 v1, v0, v1
	v_ashrrev_i32_e32 v12, 10, v1
	v_mul_i32_i24_e32 v1, 0x400, v12
	v_sub_u32_e32 v0, v0, v1
	s_load_dwordx2 s[2:3], s[10:11], 0x98
	v_and_b32_e32 v2, 24, v2
	v_and_b32_e32 v5, 4, v5
	v_lshrrev_b32_e32 v1, 4, v0
	v_or3_b32 v2, v6, v5, v2
	v_bitop3_b32 v0, v1, v0, 32 bitop3:0x6c
	v_lshl_add_u32 v136, v2, 11, v3
	v_ashrrev_i32_e32 v2, 31, v0
	v_lshrrev_b32_e32 v2, 26, v2
	v_add_u32_e32 v2, v0, v2
	s_waitcnt lgkmcnt(0)
	s_add_u32 s64, s2, 0x9f73000
	v_lshlrev_b32_e32 v1, 3, v12
	v_ashrrev_i32_e32 v13, 6, v2
	v_and_b32_e32 v2, 0xc0, v2
	s_addc_u32 s65, s3, 0
	v_and_b32_e32 v1, -16, v1
	v_sub_u32_e32 v0, v0, v2
	s_add_u32 s66, s2, 0x27b000
	v_add_u32_e32 v1, v13, v1
	v_ashrrev_i16_sdwa v0, v4, sext(v0) dst_sel:DWORD dst_unused:UNUSED_PAD src0_sel:DWORD src1_sel:BYTE_0
	v_and_b32_e32 v4, 3, v13
	s_addc_u32 s67, s3, 0
	v_and_or_b32 v4, v1, s9, v4
	s_ashr_i32 s18, s20, 6
	s_ashr_i32 s55, s54, 31
	s_ashr_i32 s9, s8, 31
	s_ashr_i32 s21, s20, 8
	s_lshl_b32 s68, s18, 10
	s_lshl_b64 s[12:13], s[54:55], 19
	s_lshl_b64 s[14:15], s[8:9], 19
	s_add_u32 s58, s66, s14
	v_lshlrev_b32_e32 v3, 5, v12
	v_bfe_i32 v14, v0, 0, 16
	v_lshlrev_b32_e32 v0, 1, v1
	v_lshrrev_b32_e32 v2, 2, v1
	s_addc_u32 s59, s67, s15
	s_add_i32 s69, s68, 0
	v_and_b32_e32 v3, 32, v3
	v_and_b32_e32 v0, 24, v0
	v_and_b32_e32 v2, 4, v2
	s_add_i32 m0, s69, 0x10000
	v_or3_b32 v0, v4, v2, v0
	v_add_lshl_u32 v2, v3, v14, 1
	global_load_lds_dwordx4 v136, s[58:59]
	s_add_i32 m0, s69, 0x12000
	v_lshl_add_u32 v142, v0, 11, v2
	s_add_u32 s14, s58, 0x40000
	global_load_lds_dwordx4 v142, s[58:59]
	s_addc_u32 s15, s59, 0
	s_add_i32 m0, s69, 0x14000
	v_lshl_add_u32 v144, v1, 11, v2
	global_load_lds_dwordx4 v136, s[14:15]
	s_add_i32 m0, s69, 0x16000
	s_add_u32 s56, s64, s12
	global_load_lds_dwordx4 v142, s[14:15]
	s_addc_u32 s57, s65, s13
	v_readfirstlane_b32 s100, v186
	s_nop 0
	s_cmp_lg_u32 s100, 0
	s_cbranch_scc1 .Lgd_p2_skip
	s_cmp_eq_u32 s98, 0
	s_cbranch_scc1 .Lgd_p2_skip
	v_readlane_b32 s100, v235, 7
	v_readlane_b32 s101, v235, 8
	v_mov_b32_e32 v236, 0x3400
	v_mov_b32_e32 v239, 0
	s_nop 3

.Lgd_p2_skip:
	s_barrier
	s_mov_b32 m0, s69
	s_add_i32 s70, s69, 0x2000
	global_load_lds_dwordx4 v138, s[56:57]
	s_mov_b32 m0, s70
	s_add_i32 s71, s69, 0x4000
	v_add_u32_e32 v140, 0x40000, v138
	global_load_lds_dwordx4 v144, s[56:57]
	s_mov_b32 m0, s71
	s_add_i32 s72, s69, 0x6000
	v_add_u32_e32 v146, 0x40000, v144
	global_load_lds_dwordx4 v140, s[56:57]
	s_mov_b32 m0, s72
	v_mov_b32_e32 v149, 0
	global_load_lds_dwordx4 v146, s[56:57]
	v_mov_b32_e32 v137, v149
	v_mov_b32_e32 v143, v149
	v_mov_b32_e32 v139, v149
	v_mov_b32_e32 v145, v149
	s_cmp_eq_u32 s21, 1
	s_mov_b32 s9, 0x40000
	s_mov_b32 s73, 0
	v_lshl_add_u64 v[6:7], s[58:59], 0, v[136:137]
	v_lshl_add_u64 v[2:3], s[58:59], 0, v[142:143]
	s_mov_b64 s[12:13], 0x40000
	v_lshl_add_u64 v[0:1], s[56:57], 0, v[138:139]
	s_cselect_b64 s[14:15], -1, 0
	s_cmp_lg_u32 s21, 1
	v_lshl_add_u64 v[4:5], s[56:57], 0, v[144:145]
	s_cbranch_scc1 .LBB0_214
	s_barrier

.LBB0_1168:
	s_or_b64 exec, exec, s[0:1]
	v_readlane_b32 s0, v235, 16
	v_readlane_b32 s1, v235, 17
	s_cmpk_lt_i32 s0, 0x200
	v_readlane_b32 s0, v235, 14
	v_readlane_b32 s1, v235, 15
	v_mov_b32_e32 v8, v186
	s_waitcnt lgkmcnt(0)
	s_barrier
	s_nop 0
	v_readfirstlane_b32 s14, v8
	s_cbranch_scc0 .LBB0_1188
	v_lshlrev_b32_e32 v0, 4, v8
	v_add_u32_e32 v1, 0x2000, v0
	v_ashrrev_i32_e32 v2, 31, v1
	v_lshrrev_b32_e32 v2, 22, v2
	v_add_u32_e32 v2, v1, v2
	v_ashrrev_i32_e32 v10, 10, v2
	v_lshlrev_b32_e32 v2, 5, v10
	v_and_b32_e32 v9, 32, v2
	v_mul_i32_i24_e32 v2, 0x400, v10
	v_sub_u32_e32 v1, v1, v2
	v_lshrrev_b32_e32 v2, 4, v1
	v_bitop3_b32 v1, v2, v1, 32 bitop3:0x6c
	v_ashrrev_i32_e32 v2, 31, v1
	v_lshrrev_b32_e32 v2, 26, v2
	v_add_u32_e32 v2, v1, v2
	v_ashrrev_i32_e32 v12, 6, v2
	v_and_b32_e32 v2, 0xc0, v2
	v_lshlrev_b32_e32 v3, 3, v10
	v_sub_u32_e32 v1, v1, v2
	v_mov_b32_e32 v2, 1
	v_and_b32_e32 v3, -16, v3
	v_ashrrev_i16_sdwa v11, v2, sext(v1) dst_sel:DWORD dst_unused:UNUSED_PAD src0_sel:DWORD src1_sel:BYTE_0
	v_add_u32_e32 v3, v12, v3
	s_movk_i32 s16, 0x580
	v_add_u32_sdwa v1, v9, sext(v11) dst_sel:DWORD dst_unused:UNUSED_PAD src0_sel:DWORD src1_sel:WORD_0
	v_mul_lo_u32 v4, v3, s16
	v_add_lshl_u32 v160, v1, v4, 1
	v_ashrrev_i32_e32 v4, 31, v8
	v_lshrrev_b32_e32 v4, 26, v4
	v_add_u32_e32 v4, v8, v4
	v_ashrrev_i32_e32 v14, 6, v4
	v_lshlrev_b32_e32 v4, 5, v14
	v_and_b32_e32 v13, 32, v4
	v_bfe_i32 v4, v8, 27, 1
	v_lshrrev_b32_e32 v4, 22, v4
	v_add_u32_e32 v4, v0, v4
	v_and_b32_e32 v4, 0xfffffc00, v4
	v_sub_u32_e32 v0, v0, v4
	v_lshrrev_b32_e32 v4, 4, v0
	v_bitop3_b32 v4, v4, v0, 32 bitop3:0x6c
	v_ashrrev_i32_e32 v0, 31, v0
	v_lshrrev_b32_e32 v0, 26, v0
	v_add_u32_e32 v0, v4, v0
	v_ashrrev_i32_e32 v16, 6, v0
	v_mul_i32_i24_e32 v0, 64, v16
	v_sub_u32_e32 v0, v4, v0
	v_ashrrev_i16_sdwa v15, v2, sext(v0) dst_sel:DWORD dst_unused:UNUSED_PAD src0_sel:DWORD src1_sel:BYTE_0
	v_lshlrev_b32_e32 v2, 3, v14
	v_and_b32_e32 v2, -16, v2
	s_load_dwordx2 s[6:7], s[0:1], 0x98
	v_add_u32_e32 v2, v16, v2
	v_add_u32_sdwa v0, v13, sext(v15) dst_sel:DWORD dst_unused:UNUSED_PAD src0_sel:DWORD src1_sel:WORD_0
	v_mul_lo_u32 v4, v2, s16
	v_add_lshl_u32 v164, v0, v4, 1
	v_and_b32_e32 v4, 3, v12
	s_mov_b32 s2, 0x1ffffe0
	s_lshl_b32 s0, s47, 3
	v_and_or_b32 v4, v3, s2, v4
	v_lshrrev_b32_e32 v5, 2, v3
	v_lshlrev_b32_e32 v3, 1, v3
	s_or_b32 s59, s0, s46
	v_and_b32_e32 v5, 4, v5
	v_and_b32_e32 v3, 24, v3
	s_waitcnt lgkmcnt(0)
	s_add_u32 s23, s6, 0x11173000
	v_or3_b32 v3, v4, v5, v3
	s_addc_u32 s33, s7, 0
	v_mul_lo_u32 v3, v3, s16
	s_add_u32 s36, s6, 0x7373000
	v_add_lshl_u32 v168, v3, v1, 1
	v_and_b32_e32 v1, 3, v16
	s_addc_u32 s37, s7, 0
	s_ashr_i32 s12, s14, 6
	v_and_or_b32 v1, v2, s2, v1
	v_lshrrev_b32_e32 v3, 2, v2
	v_lshlrev_b32_e32 v2, 1, v2
	s_ashr_i32 s15, s14, 8
	s_lshl_b32 s38, s12, 10
	s_mul_i32 s0, s22, 0xb0000
	v_and_b32_e32 v3, 4, v3
	v_and_b32_e32 v2, 24, v2
	s_mul_hi_i32 s1, s22, 0xb0000
	v_or3_b32 v1, v1, v3, v2
	s_add_u32 s0, s36, s0
	v_mul_lo_u32 v1, v1, s16
	s_addc_u32 s1, s37, s1
	s_add_i32 s39, s38, 0
	v_add_lshl_u32 v170, v1, v0, 1
	v_mov_b32_e32 v188, 0x79797979
	v_mov_b32_e32 v189, 0x7c7c7c7c
	s_add_i32 m0, s39, 0x10000
	s_mul_i32 s5, s59, 0xb0000
	global_load_lds_dwordx4 v170, s[0:1]
	s_add_i32 m0, s39, 0x12000
	s_add_u32 s2, s0, 0x58000
	global_load_lds_dwordx4 v168, s[0:1]
	s_addc_u32 s3, s1, 0
	s_add_i32 m0, s39, 0x14000
	s_mul_hi_i32 s4, s59, 0xb0000
	global_load_lds_dwordx4 v170, s[2:3]
	s_add_i32 m0, s39, 0x16000
	s_add_u32 s28, s23, s5
	global_load_lds_dwordx4 v168, s[2:3]
	s_addc_u32 s29, s33, s4
	v_readfirstlane_b32 s100, v186
	s_nop 0
	s_cmp_lg_u32 s100, 0
	s_cbranch_scc1 .Lgd_p10_skip
	s_cmp_eq_u32 s98, 0
	s_cbranch_scc1 .Lgd_p10_skip
	v_readlane_b32 s100, v235, 7
	v_readlane_b32 s101, v235, 8
	v_mov_b32_e32 v236, 0x3400
	v_mov_b32_e32 v239, 0
	s_nop 3

.Lgd_p10_skip:
	s_barrier
	s_mov_b32 m0, s39
	s_add_i32 s40, s39, 0x2000
	global_load_lds_dwordx4 v164, s[28:29]
	s_mov_b32 m0, s40
	s_add_i32 s41, s39, 0x4000
	v_add_u32_e32 v166, 0x58000, v164
	global_load_lds_dwordx4 v160, s[28:29]
	s_mov_b32 m0, s41
	s_add_i32 s42, s39, 0x6000
	v_add_u32_e32 v162, 0x58000, v160
	global_load_lds_dwordx4 v166, s[28:29]
	s_mov_b32 m0, s42
	v_mov_b32_e32 v173, 0
	global_load_lds_dwordx4 v162, s[28:29]
	v_mov_b32_e32 v171, v173
	v_mov_b32_e32 v169, v173
	v_mov_b32_e32 v165, v173
	v_mov_b32_e32 v161, v173
	s_cmp_eq_u32 s15, 1
	s_mov_b32 s43, 0x58000
	s_mov_b32 s44, 0
	v_lshl_add_u64 v[6:7], s[0:1], 0, v[170:171]
	v_lshl_add_u64 v[2:3], s[0:1], 0, v[168:169]
	s_mov_b64 s[2:3], 0x58000
	v_lshl_add_u64 v[0:1], s[28:29], 0, v[164:165]
	s_cselect_b64 s[4:5], -1, 0
	s_cmp_lg_u32 s15, 1
	v_lshl_add_u64 v[4:5], s[28:29], 0, v[160:161]
	s_cbranch_scc1 .LBB0_1171
	s_barrier
